# C2 epilogue: 10 false-hazard s_nop between dependent packed-f32 ops removed (same class as the O1 epilogue edit), on the window-fill variant
# speedup vs baseline: 1.0013x; 1.0013x over previous
; #define LAS __attribute__((address_space(3)))
; template <bool EMU> __device__ __forceinline__ float e2m3q(float y) { if constexpr (EMU) { y = fminf(fmaxf(y, -7.5f), 7.5f); return fabsf(y) < 1.f ? rintf(y * 8.f) * 0.125f : y; } else return y; }
;     static __device__ __forceinline__ f32x2 act2(f32x2 g, f32x2 l) {
;         g = __builtin_elementwise_min(g, (f32x2){7.f, 7.f}); l = __builtin_elementwise_min(__builtin_elementwise_max(l, (f32x2){-7.f, -7.f}), (f32x2){7.f, 7.f});
;         const f32x2 t = g * (-1.702f * 1.44269504089f); f32x2 e; e.x = __builtin_amdgcn_exp2f(t.x); e.y = __builtin_amdgcn_exp2f(t.y);
;         const f32x2 d = e + 1.0f; f32x2 r; r.x = __builtin_amdgcn_rcpf(d.x); r.y = __builtin_amdgcn_rcpf(d.y);
;         return (g * r) * (l * QS_ACT + QS_ACT);
;     }
;     __device__ __forceinline__ void operator()(const f32x4 (&acc)[2][2][4][2], const UnitD& u, int wr, int wc, int fr, int fq) const {
;         const int row0 = u.r0 + wr * 64 + fr, col0 = u.c0 + wc * 32 + 8 * fq;
;         const LAS float* bg = bl_lds + u.ui * 256 + wc * 32 + 8 * fq; const LAS float* bl = bg + 128;
;         f32x4 bgv[2], blv[2];
; #pragma unroll
;         for (int n = 0; n < 2; ++n) { bgv[n] = *(const LAS f32x4*)(bg + 4 * n); blv[n] = *(const LAS f32x4*)(bl + 4 * n); }
;         constexpr float SC = 1.f / (QS_X1 * QS_WUP);
; #pragma unroll
;         for (int ai = 0; ai < 2; ++ai)
; #pragma unroll
;             for (int m = 0; m < 4; ++m) { unsigned char* rowp = H + (size_t)(row0 + ai * 128 + m * 16) * DM + col0; u32x2 w;
; #pragma unroll
;                 for (int n = 0; n < 2; ++n) { const f32x4 g = acc[ai][0][m][n] * SC + bgv[n], l = acc[ai][1][m][n] * SC + blv[n];
;                     const f32x2 o0 = act2((f32x2){g[0], g[1]}, (f32x2){l[0], l[1]}), o1 = act2((f32x2){g[2], g[3]}, (f32x2){l[2], l[3]});
;                     int r = 0; r = __builtin_amdgcn_cvt_pk_fp8_f32(e2m3q<EMU_DOWN != 0>(o0.x), e2m3q<EMU_DOWN != 0>(o0.y), r, false); r = __builtin_amdgcn_cvt_pk_fp8_f32(e2m3q<EMU_DOWN != 0>(o1.x), e2m3q<EMU_DOWN != 0>(o1.y), r, true);
;                     if (n == 0) w.x = (unsigned)r; else w.y = (unsigned)r; }
;                 *(u32x2*)rowp = w; }
.LBB0_755:
	s_add_u32 s18, s85, 0xffffff00
	v_mov_b32_e32 v16, v154
	v_bfe_u32 v152, v154, 4, 1
	s_addc_u32 s19, s86, -1
	s_lshl_b32 s20, s76, 10
	v_mul_u32_u24_e32 v152, 0x3ff8, v152
	v_lshrrev_b32_e32 v0, 1, v16
	v_and_b32_e32 v18, 0x60, v0
	v_and_b32_e32 v19, 24, v0
	s_add_i32 s20, s20, 0
	s_add_i32 s20, s20, 0x23100
	v_lshlrev_b32_e32 v0, 2, v18
	v_lshlrev_b32_e32 v1, 2, v19
	v_add3_u32 v4, s20, v0, v1
	ds_read_b128 v[8:11], v4
	ds_read_b128 v[0:3], v4 offset:16
	ds_read_b128 v[12:15], v4 offset:512
	ds_read_b128 v[4:7], v4 offset:528
	v_and_b32_e32 v17, 15, v16
	s_waitcnt lgkmcnt(0)
	v_pk_fma_f32 v[22:23], v[148:149], s[36:37], v[8:9] op_sel_hi:[1,0,1]
	v_ashrrev_i32_e32 v20, 2, v16
	v_min_f32_e32 v23, 0x40e00000, v23
	v_min_f32_e32 v22, 0x40e00000, v22
	v_pk_mul_f32 v[176:177], v[22:23], s[78:79] op_sel_hi:[1,0]
	v_pk_fma_f32 v[174:175], v[116:117], s[36:37], v[12:13] op_sel_hi:[1,0,1]
	v_exp_f32_e32 v176, v176
	v_exp_f32_e32 v177, v177
	v_and_or_b32 v17, v20, s39, v17
	v_pk_fma_f32 v[20:21], v[150:151], s[36:37], v[10:11] op_sel_hi:[1,0,1]
	v_med3_f32 v175, v175, s47, v190
	v_pk_add_f32 v[176:177], v[176:177], 1.0 op_sel_hi:[1,0]
	v_med3_f32 v174, v174, s47, v190
	v_rcp_f32_e32 v176, v176
	v_rcp_f32_e32 v177, v177
	v_pk_fma_f32 v[174:175], v[174:175], 4.0, 4.0 op_sel_hi:[1,0,0]
	v_min_f32_e32 v21, 0x40e00000, v21
	v_min_f32_e32 v20, 0x40e00000, v20
	v_pk_mul_f32 v[22:23], v[22:23], v[176:177]
	v_pk_fma_f32 v[172:173], v[118:119], s[36:37], v[14:15] op_sel_hi:[1,0,1]
	v_pk_mul_f32 v[22:23], v[174:175], v[22:23]
	v_pk_mul_f32 v[174:175], v[20:21], s[78:79] op_sel_hi:[1,0]
	v_med3_f32 v173, v173, s47, v190
	v_exp_f32_e32 v174, v174
	v_exp_f32_e32 v175, v175
	v_med3_f32 v172, v172, s47, v190
	v_pk_fma_f32 v[172:173], v[172:173], 4.0, 4.0 op_sel_hi:[1,0,0]
	v_pk_fma_f32 v[176:177], v[112:113], s[36:37], v[4:5] op_sel_hi:[1,0,1]
	v_pk_add_f32 v[174:175], v[174:175], 1.0 op_sel_hi:[1,0]
	v_med3_f32 v177, v177, s47, v190
	v_rcp_f32_e32 v174, v174
	v_rcp_f32_e32 v175, v175
	v_med3_f32 v176, v176, s47, v190
	v_pk_fma_f32 v[176:177], v[176:177], 4.0, 4.0 op_sel_hi:[1,0,0]
	v_add3_u32 v16, v18, s2, v19
	v_pk_mul_f32 v[20:21], v[20:21], v[174:175]
	v_pk_fma_f32 v[174:175], v[114:115], s[36:37], v[6:7] op_sel_hi:[1,0,1]
	v_pk_mul_f32 v[20:21], v[172:173], v[20:21]
	v_cvt_pk_fp8_f32 v148, v22, v23
	v_pk_fma_f32 v[22:23], v[144:145], s[36:37], v[0:1] op_sel_hi:[1,0,1]
	v_min_f32_e32 v23, 0x40e00000, v23
	v_min_f32_e32 v22, 0x40e00000, v22
	v_pk_mul_f32 v[178:179], v[22:23], s[78:79] op_sel_hi:[1,0]
	v_cvt_pk_fp8_f32 v148, v20, v21 op_sel:[0,0,1]
	v_exp_f32_e32 v178, v178
	v_exp_f32_e32 v179, v179
	v_pk_fma_f32 v[20:21], v[146:147], s[36:37], v[2:3] op_sel_hi:[1,0,1]
	v_med3_f32 v175, v175, s47, v190
	v_min_f32_e32 v21, 0x40e00000, v21
	v_pk_add_f32 v[178:179], v[178:179], 1.0 op_sel_hi:[1,0]
	v_min_f32_e32 v20, 0x40e00000, v20
	v_rcp_f32_e32 v178, v178
	v_rcp_f32_e32 v179, v179
	v_med3_f32 v174, v174, s47, v190
	v_pk_fma_f32 v[174:175], v[174:175], 4.0, 4.0 op_sel_hi:[1,0,0]
	v_add_u32_e32 v18, s68, v17
	v_pk_mul_f32 v[22:23], v[22:23], v[178:179]
	v_ashrrev_i32_e32 v19, 31, v18
	v_pk_mul_f32 v[22:23], v[176:177], v[22:23]
	v_pk_mul_f32 v[176:177], v[20:21], s[78:79] op_sel_hi:[1,0]
	v_cvt_pk_fp8_f32 v149, v22, v23
	v_exp_f32_e32 v176, v176
	v_exp_f32_e32 v177, v177
	v_lshlrev_b64 v[18:19], 10, v[18:19]
	v_ashrrev_i32_e32 v17, 31, v16
	v_lshl_add_u64 v[18:19], s[6:7], 0, v[18:19]
	v_pk_add_f32 v[176:177], v[176:177], 1.0 op_sel_hi:[1,0]
	v_lshl_add_u64 v[16:17], v[18:19], 0, v[16:17]
	s_nop 0
	v_lshl_add_u64 v[144:145], v[16:17], 0, v[152:153]
	v_rcp_f32_e32 v176, v176
	v_rcp_f32_e32 v177, v177
	v_pk_fma_f32 v[18:19], v[142:143], s[36:37], v[10:11] op_sel_hi:[1,0,1]
	v_pk_fma_f32 v[22:23], v[110:111], s[36:37], v[14:15] op_sel_hi:[1,0,1]
	v_min_f32_e32 v19, 0x40e00000, v19
	v_pk_mul_f32 v[20:21], v[20:21], v[176:177]
	v_min_f32_e32 v18, 0x40e00000, v18
	v_pk_mul_f32 v[20:21], v[174:175], v[20:21]
	v_med3_f32 v23, v23, s47, v190
	v_cvt_pk_fp8_f32 v149, v20, v21 op_sel:[0,0,1]
	v_pk_fma_f32 v[20:21], v[140:141], s[36:37], v[8:9] op_sel_hi:[1,0,1]
	v_med3_f32 v22, v22, s47, v190
	v_min_f32_e32 v21, 0x40e00000, v21
	v_min_f32_e32 v20, 0x40e00000, v20
	v_pk_mul_f32 v[174:175], v[20:21], s[78:79] op_sel_hi:[1,0]
	v_exp_f32_e32 v174, v174
	v_exp_f32_e32 v175, v175
	v_pk_fma_f32 v[172:173], v[108:109], s[36:37], v[12:13] op_sel_hi:[1,0,1]
	v_pk_fma_f32 v[22:23], v[22:23], 4.0, 4.0 op_sel_hi:[1,0,0]
	v_med3_f32 v173, v173, s47, v190
	v_pk_add_f32 v[174:175], v[174:175], 1.0 op_sel_hi:[1,0]
	v_med3_f32 v172, v172, s47, v190
	v_rcp_f32_e32 v174, v174
	v_rcp_f32_e32 v175, v175
	v_pk_fma_f32 v[172:173], v[172:173], 4.0, 4.0 op_sel_hi:[1,0,0]
	s_movk_i32 s20, 0x4000
	s_mov_b64 s[88:89], 0x42040080
	v_pk_mul_f32 v[20:21], v[20:21], v[174:175]
	v_pk_fma_f32 v[174:175], v[104:105], s[36:37], v[4:5] op_sel_hi:[1,0,1]
	v_pk_mul_f32 v[20:21], v[172:173], v[20:21]
	v_pk_mul_f32 v[172:173], v[18:19], s[78:79] op_sel_hi:[1,0]
	v_med3_f32 v175, v175, s47, v190
	v_exp_f32_e32 v172, v172
	v_exp_f32_e32 v173, v173
	v_med3_f32 v174, v174, s47, v190
	v_pk_fma_f32 v[174:175], v[174:175], 4.0, 4.0 op_sel_hi:[1,0,0]
	v_pk_add_f32 v[172:173], v[172:173], 1.0 op_sel_hi:[1,0]
	s_nop 0
	v_rcp_f32_e32 v172, v172
	v_rcp_f32_e32 v173, v173
	s_nop 0
	v_pk_mul_f32 v[18:19], v[18:19], v[172:173]
	v_pk_mul_f32 v[18:19], v[22:23], v[18:19]
	v_cvt_pk_fp8_f32 v150, v20, v21
	v_pk_fma_f32 v[20:21], v[136:137], s[36:37], v[0:1] op_sel_hi:[1,0,1]
	v_min_f32_e32 v21, 0x40e00000, v21
	v_min_f32_e32 v20, 0x40e00000, v20
	v_pk_mul_f32 v[176:177], v[20:21], s[78:79] op_sel_hi:[1,0]
; #define LAS __attribute__((address_space(3)))
; template <bool EMU> __device__ __forceinline__ float e2m3q(float y) { if constexpr (EMU) { y = fminf(fmaxf(y, -7.5f), 7.5f); return fabsf(y) < 1.f ? rintf(y * 8.f) * 0.125f : y; } else return y; }
;     static __device__ __forceinline__ f32x2 act2(f32x2 g, f32x2 l) {
;         g = __builtin_elementwise_min(g, (f32x2){7.f, 7.f}); l = __builtin_elementwise_min(__builtin_elementwise_max(l, (f32x2){-7.f, -7.f}), (f32x2){7.f, 7.f});
;         const f32x2 t = g * (-1.702f * 1.44269504089f); f32x2 e; e.x = __builtin_amdgcn_exp2f(t.x); e.y = __builtin_amdgcn_exp2f(t.y);
;         const f32x2 d = e + 1.0f; f32x2 r; r.x = __builtin_amdgcn_rcpf(d.x); r.y = __builtin_amdgcn_rcpf(d.y);
;         return (g * r) * (l * QS_ACT + QS_ACT);
;     }
;     __device__ __forceinline__ void operator()(const f32x4 (&acc)[2][2][4][2], const UnitD& u, int wr, int wc, int fr, int fq) const {
;         const int row0 = u.r0 + wr * 64 + fr, col0 = u.c0 + wc * 32 + 8 * fq;
;         const LAS float* bg = bl_lds + u.ui * 256 + wc * 32 + 8 * fq; const LAS float* bl = bg + 128;
;         f32x4 bgv[2], blv[2];
; #pragma unroll
;         for (int n = 0; n < 2; ++n) { bgv[n] = *(const LAS f32x4*)(bg + 4 * n); blv[n] = *(const LAS f32x4*)(bl + 4 * n); }
;         constexpr float SC = 1.f / (QS_X1 * QS_WUP);
; #pragma unroll
;         for (int ai = 0; ai < 2; ++ai)
; #pragma unroll
;             for (int m = 0; m < 4; ++m) { unsigned char* rowp = H + (size_t)(row0 + ai * 128 + m * 16) * DM + col0; u32x2 w;
; #pragma unroll
;                 for (int n = 0; n < 2; ++n) { const f32x4 g = acc[ai][0][m][n] * SC + bgv[n], l = acc[ai][1][m][n] * SC + blv[n];
;                     const f32x2 o0 = act2((f32x2){g[0], g[1]}, (f32x2){l[0], l[1]}), o1 = act2((f32x2){g[2], g[3]}, (f32x2){l[2], l[3]});
;                     int r = 0; r = __builtin_amdgcn_cvt_pk_fp8_f32(e2m3q<EMU_DOWN != 0>(o0.x), e2m3q<EMU_DOWN != 0>(o0.y), r, false); r = __builtin_amdgcn_cvt_pk_fp8_f32(e2m3q<EMU_DOWN != 0>(o1.x), e2m3q<EMU_DOWN != 0>(o1.y), r, true);
;                     if (n == 0) w.x = (unsigned)r; else w.y = (unsigned)r; }
;                 *(u32x2*)rowp = w; }
	v_cvt_pk_fp8_f32 v150, v18, v19 op_sel:[0,0,1]
	v_exp_f32_e32 v176, v176
	v_exp_f32_e32 v177, v177
	v_pk_fma_f32 v[18:19], v[138:139], s[36:37], v[2:3] op_sel_hi:[1,0,1]
	v_pk_fma_f32 v[172:173], v[106:107], s[36:37], v[6:7] op_sel_hi:[1,0,1]
	v_min_f32_e32 v19, 0x40e00000, v19
	v_pk_add_f32 v[176:177], v[176:177], 1.0 op_sel_hi:[1,0]
	v_min_f32_e32 v18, 0x40e00000, v18
	v_rcp_f32_e32 v176, v176
	v_rcp_f32_e32 v177, v177
	v_med3_f32 v173, v173, s47, v190
	v_med3_f32 v172, v172, s47, v190
	v_pk_fma_f32 v[172:173], v[172:173], 4.0, 4.0 op_sel_hi:[1,0,0]
	v_pk_mul_f32 v[20:21], v[20:21], v[176:177]
	v_pk_mul_f32 v[20:21], v[174:175], v[20:21]
	v_pk_mul_f32 v[174:175], v[18:19], s[78:79] op_sel_hi:[1,0]
	v_cvt_pk_fp8_f32 v151, v20, v21
	v_exp_f32_e32 v174, v174
	v_exp_f32_e32 v175, v175
	v_pk_fma_f32 v[20:21], v[132:133], s[36:37], v[8:9] op_sel_hi:[1,0,1]
	v_pk_add_f32 v[174:175], v[174:175], 1.0 op_sel_hi:[1,0]
	s_nop 0
	v_rcp_f32_e32 v174, v174
	v_rcp_f32_e32 v175, v175
	v_min_f32_e32 v21, 0x40e00000, v21
	v_min_f32_e32 v20, 0x40e00000, v20
	v_pk_mul_f32 v[18:19], v[18:19], v[174:175]
	v_pk_mul_f32 v[174:175], v[20:21], s[78:79] op_sel_hi:[1,0]
	v_pk_mul_f32 v[18:19], v[172:173], v[18:19]
	v_exp_f32_e32 v174, v174
	v_exp_f32_e32 v175, v175
	v_cvt_pk_fp8_f32 v151, v18, v19 op_sel:[0,0,1]
	v_add_co_u32_e32 v18, vcc, s20, v16
	v_pk_add_f32 v[174:175], v[174:175], 1.0 op_sel_hi:[1,0]
	s_nop 0
	v_addc_co_u32_e32 v19, vcc, 0, v17, vcc
	v_rcp_f32_e32 v174, v174
	v_rcp_f32_e32 v175, v175
	v_pk_fma_f32 v[172:173], v[100:101], s[36:37], v[12:13] op_sel_hi:[1,0,1]
	v_permlane16_swap_b32_e32 v148, v150
	v_permlane16_swap_b32_e32 v149, v151
	global_store_dwordx4 v[144:145], v[148:151], off
	v_pk_fma_f32 v[18:19], v[134:135], s[36:37], v[10:11] op_sel_hi:[1,0,1]
	v_med3_f32 v173, v173, s47, v190
	v_med3_f32 v172, v172, s47, v190
	v_pk_mul_f32 v[20:21], v[20:21], v[174:175]
	v_pk_fma_f32 v[172:173], v[172:173], 4.0, 4.0 op_sel_hi:[1,0,0]
	v_min_f32_e32 v19, 0x40e00000, v19
	v_min_f32_e32 v18, 0x40e00000, v18
	v_pk_mul_f32 v[20:21], v[172:173], v[20:21]
	v_pk_mul_f32 v[172:173], v[18:19], s[78:79] op_sel_hi:[1,0]
	v_pk_fma_f32 v[22:23], v[102:103], s[36:37], v[14:15] op_sel_hi:[1,0,1]
	v_exp_f32_e32 v172, v172
	v_exp_f32_e32 v173, v173
	v_med3_f32 v23, v23, s47, v190
	v_med3_f32 v22, v22, s47, v190
	v_pk_fma_f32 v[22:23], v[22:23], 4.0, 4.0 op_sel_hi:[1,0,0]
	v_pk_add_f32 v[172:173], v[172:173], 1.0 op_sel_hi:[1,0]
	v_pk_fma_f32 v[174:175], v[96:97], s[36:37], v[4:5] op_sel_hi:[1,0,1]
	v_rcp_f32_e32 v172, v172
	v_rcp_f32_e32 v173, v173
	v_med3_f32 v175, v175, s47, v190
	v_med3_f32 v174, v174, s47, v190
	v_pk_fma_f32 v[174:175], v[174:175], 4.0, 4.0 op_sel_hi:[1,0,0]
	v_pk_mul_f32 v[18:19], v[18:19], v[172:173]
	v_pk_fma_f32 v[172:173], v[98:99], s[36:37], v[6:7] op_sel_hi:[1,0,1]
	v_pk_mul_f32 v[18:19], v[22:23], v[18:19]
	v_cvt_pk_fp8_f32 v148, v20, v21
	v_pk_fma_f32 v[20:21], v[128:129], s[36:37], v[0:1] op_sel_hi:[1,0,1]
	v_min_f32_e32 v21, 0x40e00000, v21
	v_min_f32_e32 v20, 0x40e00000, v20
	v_pk_mul_f32 v[176:177], v[20:21], s[78:79] op_sel_hi:[1,0]
	v_cvt_pk_fp8_f32 v148, v18, v19 op_sel:[0,0,1]
	v_exp_f32_e32 v176, v176
	v_exp_f32_e32 v177, v177
	v_pk_fma_f32 v[18:19], v[130:131], s[36:37], v[2:3] op_sel_hi:[1,0,1]
	v_med3_f32 v173, v173, s47, v190
	v_min_f32_e32 v19, 0x40e00000, v19
	v_pk_add_f32 v[176:177], v[176:177], 1.0 op_sel_hi:[1,0]
	v_min_f32_e32 v18, 0x40e00000, v18
	v_rcp_f32_e32 v176, v176
	v_rcp_f32_e32 v177, v177
	v_med3_f32 v172, v172, s47, v190
	v_pk_fma_f32 v[172:173], v[172:173], 4.0, 4.0 op_sel_hi:[1,0,0]
	s_mov_b32 s20, 0x8000
	v_pk_mul_f32 v[20:21], v[20:21], v[176:177]
	v_pk_mul_f32 v[20:21], v[174:175], v[20:21]
	v_pk_mul_f32 v[174:175], v[18:19], s[78:79] op_sel_hi:[1,0]
	v_cvt_pk_fp8_f32 v149, v20, v21
	v_exp_f32_e32 v174, v174
	v_exp_f32_e32 v175, v175
	v_pk_fma_f32 v[20:21], v[124:125], s[36:37], v[8:9] op_sel_hi:[1,0,1]
	v_pk_add_f32 v[174:175], v[174:175], 1.0 op_sel_hi:[1,0]
	s_nop 0
	v_rcp_f32_e32 v174, v174
	v_rcp_f32_e32 v175, v175
	v_min_f32_e32 v21, 0x40e00000, v21
	v_min_f32_e32 v20, 0x40e00000, v20
	v_pk_mul_f32 v[18:19], v[18:19], v[174:175]
	v_pk_mul_f32 v[174:175], v[20:21], s[78:79] op_sel_hi:[1,0]
	v_pk_mul_f32 v[18:19], v[172:173], v[18:19]
	v_exp_f32_e32 v174, v174
	v_exp_f32_e32 v175, v175
	v_cvt_pk_fp8_f32 v149, v18, v19 op_sel:[0,0,1]
	v_add_co_u32_e32 v18, vcc, s20, v16
	v_pk_add_f32 v[174:175], v[174:175], 1.0 op_sel_hi:[1,0]
	s_nop 0
	v_addc_co_u32_e32 v19, vcc, 0, v17, vcc
	v_rcp_f32_e32 v174, v174
	v_rcp_f32_e32 v175, v175
	v_pk_fma_f32 v[172:173], v[92:93], s[36:37], v[12:13] op_sel_hi:[1,0,1]
	v_lshl_add_u64 v[146:147], v[18:19], 0, v[152:153]
	v_pk_fma_f32 v[18:19], v[126:127], s[36:37], v[10:11] op_sel_hi:[1,0,1]
	v_med3_f32 v173, v173, s47, v190
	v_med3_f32 v172, v172, s47, v190
	v_pk_mul_f32 v[20:21], v[20:21], v[174:175]
	v_pk_fma_f32 v[172:173], v[172:173], 4.0, 4.0 op_sel_hi:[1,0,0]
	v_min_f32_e32 v19, 0x40e00000, v19
	v_min_f32_e32 v18, 0x40e00000, v18
	v_pk_mul_f32 v[20:21], v[172:173], v[20:21]
	v_pk_mul_f32 v[172:173], v[18:19], s[78:79] op_sel_hi:[1,0]
	v_pk_fma_f32 v[22:23], v[94:95], s[36:37], v[14:15] op_sel_hi:[1,0,1]
	v_exp_f32_e32 v172, v172
	v_exp_f32_e32 v173, v173
	v_med3_f32 v23, v23, s47, v190
	v_med3_f32 v22, v22, s47, v190
	v_pk_fma_f32 v[22:23], v[22:23], 4.0, 4.0 op_sel_hi:[1,0,0]
	v_pk_add_f32 v[172:173], v[172:173], 1.0 op_sel_hi:[1,0]
	v_pk_fma_f32 v[174:175], v[88:89], s[36:37], v[4:5] op_sel_hi:[1,0,1]
	v_rcp_f32_e32 v172, v172
	v_rcp_f32_e32 v173, v173
	v_med3_f32 v175, v175, s47, v190
	v_med3_f32 v174, v174, s47, v190
	v_pk_fma_f32 v[174:175], v[174:175], 4.0, 4.0 op_sel_hi:[1,0,0]
; #define LAS __attribute__((address_space(3)))
; template <bool EMU> __device__ __forceinline__ float e2m3q(float y) { if constexpr (EMU) { y = fminf(fmaxf(y, -7.5f), 7.5f); return fabsf(y) < 1.f ? rintf(y * 8.f) * 0.125f : y; } else return y; }
;     static __device__ __forceinline__ f32x2 act2(f32x2 g, f32x2 l) {
;         g = __builtin_elementwise_min(g, (f32x2){7.f, 7.f}); l = __builtin_elementwise_min(__builtin_elementwise_max(l, (f32x2){-7.f, -7.f}), (f32x2){7.f, 7.f});
;         const f32x2 t = g * (-1.702f * 1.44269504089f); f32x2 e; e.x = __builtin_amdgcn_exp2f(t.x); e.y = __builtin_amdgcn_exp2f(t.y);
;         const f32x2 d = e + 1.0f; f32x2 r; r.x = __builtin_amdgcn_rcpf(d.x); r.y = __builtin_amdgcn_rcpf(d.y);
;         return (g * r) * (l * QS_ACT + QS_ACT);
;     }
;     __device__ __forceinline__ void operator()(const f32x4 (&acc)[2][2][4][2], const UnitD& u, int wr, int wc, int fr, int fq) const {
;         const int row0 = u.r0 + wr * 64 + fr, col0 = u.c0 + wc * 32 + 8 * fq;
;         const LAS float* bg = bl_lds + u.ui * 256 + wc * 32 + 8 * fq; const LAS float* bl = bg + 128;
;         f32x4 bgv[2], blv[2];
; #pragma unroll
;         for (int n = 0; n < 2; ++n) { bgv[n] = *(const LAS f32x4*)(bg + 4 * n); blv[n] = *(const LAS f32x4*)(bl + 4 * n); }
;         constexpr float SC = 1.f / (QS_X1 * QS_WUP);
; #pragma unroll
;         for (int ai = 0; ai < 2; ++ai)
; #pragma unroll
;             for (int m = 0; m < 4; ++m) { unsigned char* rowp = H + (size_t)(row0 + ai * 128 + m * 16) * DM + col0; u32x2 w;
; #pragma unroll
;                 for (int n = 0; n < 2; ++n) { const f32x4 g = acc[ai][0][m][n] * SC + bgv[n], l = acc[ai][1][m][n] * SC + blv[n];
;                     const f32x2 o0 = act2((f32x2){g[0], g[1]}, (f32x2){l[0], l[1]}), o1 = act2((f32x2){g[2], g[3]}, (f32x2){l[2], l[3]});
;                     int r = 0; r = __builtin_amdgcn_cvt_pk_fp8_f32(e2m3q<EMU_DOWN != 0>(o0.x), e2m3q<EMU_DOWN != 0>(o0.y), r, false); r = __builtin_amdgcn_cvt_pk_fp8_f32(e2m3q<EMU_DOWN != 0>(o1.x), e2m3q<EMU_DOWN != 0>(o1.y), r, true);
;                     if (n == 0) w.x = (unsigned)r; else w.y = (unsigned)r; }
;                 *(u32x2*)rowp = w; }
	v_pk_mul_f32 v[18:19], v[18:19], v[172:173]
	v_pk_fma_f32 v[172:173], v[90:91], s[36:37], v[6:7] op_sel_hi:[1,0,1]
	v_pk_mul_f32 v[18:19], v[22:23], v[18:19]
	v_cvt_pk_fp8_f32 v150, v20, v21
	v_pk_fma_f32 v[20:21], v[120:121], s[36:37], v[0:1] op_sel_hi:[1,0,1]
	v_min_f32_e32 v21, 0x40e00000, v21
	v_min_f32_e32 v20, 0x40e00000, v20
	v_pk_mul_f32 v[176:177], v[20:21], s[78:79] op_sel_hi:[1,0]
	v_cvt_pk_fp8_f32 v150, v18, v19 op_sel:[0,0,1]
	v_exp_f32_e32 v176, v176
	v_exp_f32_e32 v177, v177
	v_pk_fma_f32 v[18:19], v[122:123], s[36:37], v[2:3] op_sel_hi:[1,0,1]
	v_med3_f32 v173, v173, s47, v190
	v_min_f32_e32 v19, 0x40e00000, v19
	v_pk_add_f32 v[176:177], v[176:177], 1.0 op_sel_hi:[1,0]
	v_min_f32_e32 v18, 0x40e00000, v18
	v_rcp_f32_e32 v176, v176
	v_rcp_f32_e32 v177, v177
	v_med3_f32 v172, v172, s47, v190
	v_pk_fma_f32 v[172:173], v[172:173], 4.0, 4.0 op_sel_hi:[1,0,0]
	s_mov_b32 s20, 0xc000
	v_pk_mul_f32 v[20:21], v[20:21], v[176:177]
	v_pk_mul_f32 v[20:21], v[174:175], v[20:21]
	v_pk_mul_f32 v[174:175], v[18:19], s[78:79] op_sel_hi:[1,0]
	v_cvt_pk_fp8_f32 v151, v20, v21
	v_exp_f32_e32 v174, v174
	v_exp_f32_e32 v175, v175
	v_pk_fma_f32 v[20:21], v[84:85], s[36:37], v[8:9] op_sel_hi:[1,0,1]
	v_pk_add_f32 v[174:175], v[174:175], 1.0 op_sel_hi:[1,0]
	s_nop 0
	v_rcp_f32_e32 v174, v174
	v_rcp_f32_e32 v175, v175
	v_min_f32_e32 v21, 0x40e00000, v21
	v_min_f32_e32 v20, 0x40e00000, v20
	v_pk_mul_f32 v[18:19], v[18:19], v[174:175]
	v_pk_mul_f32 v[174:175], v[20:21], s[78:79] op_sel_hi:[1,0]
	v_pk_mul_f32 v[18:19], v[172:173], v[18:19]
	v_exp_f32_e32 v174, v174
	v_exp_f32_e32 v175, v175
	v_cvt_pk_fp8_f32 v151, v18, v19 op_sel:[0,0,1]
	v_add_co_u32_e32 v18, vcc, s20, v16
	v_pk_add_f32 v[174:175], v[174:175], 1.0 op_sel_hi:[1,0]
	s_nop 0
	v_addc_co_u32_e32 v19, vcc, 0, v17, vcc
	v_rcp_f32_e32 v174, v174
	v_rcp_f32_e32 v175, v175
	v_pk_fma_f32 v[172:173], v[52:53], s[36:37], v[12:13] op_sel_hi:[1,0,1]
	v_permlane16_swap_b32_e32 v148, v150
	v_permlane16_swap_b32_e32 v149, v151
	global_store_dwordx4 v[146:147], v[148:151], off
	v_pk_fma_f32 v[18:19], v[86:87], s[36:37], v[10:11] op_sel_hi:[1,0,1]
	v_med3_f32 v173, v173, s47, v190
	v_med3_f32 v172, v172, s47, v190
	v_pk_mul_f32 v[20:21], v[20:21], v[174:175]
	v_pk_fma_f32 v[172:173], v[172:173], 4.0, 4.0 op_sel_hi:[1,0,0]
	v_min_f32_e32 v19, 0x40e00000, v19
	v_min_f32_e32 v18, 0x40e00000, v18
	v_pk_mul_f32 v[20:21], v[172:173], v[20:21]
	v_pk_mul_f32 v[172:173], v[18:19], s[78:79] op_sel_hi:[1,0]
	v_pk_fma_f32 v[22:23], v[54:55], s[36:37], v[14:15] op_sel_hi:[1,0,1]
	v_exp_f32_e32 v172, v172
	v_exp_f32_e32 v173, v173
	v_med3_f32 v23, v23, s47, v190
	v_med3_f32 v22, v22, s47, v190
	v_pk_fma_f32 v[22:23], v[22:23], 4.0, 4.0 op_sel_hi:[1,0,0]
	v_pk_add_f32 v[172:173], v[172:173], 1.0 op_sel_hi:[1,0]
	v_pk_fma_f32 v[174:175], v[48:49], s[36:37], v[4:5] op_sel_hi:[1,0,1]
	v_rcp_f32_e32 v172, v172
	v_rcp_f32_e32 v173, v173
	v_med3_f32 v175, v175, s47, v190
	v_med3_f32 v174, v174, s47, v190
	v_pk_fma_f32 v[174:175], v[174:175], 4.0, 4.0 op_sel_hi:[1,0,0]
	v_pk_mul_f32 v[18:19], v[18:19], v[172:173]
	v_pk_fma_f32 v[172:173], v[50:51], s[36:37], v[6:7] op_sel_hi:[1,0,1]
	v_pk_mul_f32 v[18:19], v[22:23], v[18:19]
	v_cvt_pk_fp8_f32 v148, v20, v21
	v_pk_fma_f32 v[20:21], v[80:81], s[36:37], v[0:1] op_sel_hi:[1,0,1]
	v_min_f32_e32 v21, 0x40e00000, v21
	v_min_f32_e32 v20, 0x40e00000, v20
	v_pk_mul_f32 v[176:177], v[20:21], s[78:79] op_sel_hi:[1,0]
	v_cvt_pk_fp8_f32 v148, v18, v19 op_sel:[0,0,1]
	v_exp_f32_e32 v176, v176
	v_exp_f32_e32 v177, v177
	v_pk_fma_f32 v[18:19], v[82:83], s[36:37], v[2:3] op_sel_hi:[1,0,1]
	v_med3_f32 v173, v173, s47, v190
	v_min_f32_e32 v19, 0x40e00000, v19
	v_pk_add_f32 v[176:177], v[176:177], 1.0 op_sel_hi:[1,0]
	v_min_f32_e32 v18, 0x40e00000, v18
	v_rcp_f32_e32 v176, v176
	v_rcp_f32_e32 v177, v177
	v_med3_f32 v172, v172, s47, v190
	v_pk_fma_f32 v[172:173], v[172:173], 4.0, 4.0 op_sel_hi:[1,0,0]
	s_mov_b32 s20, 0x20000
	v_pk_mul_f32 v[20:21], v[20:21], v[176:177]
	v_pk_mul_f32 v[20:21], v[174:175], v[20:21]
	v_pk_mul_f32 v[174:175], v[18:19], s[78:79] op_sel_hi:[1,0]
	v_cvt_pk_fp8_f32 v149, v20, v21
	v_exp_f32_e32 v174, v174
	v_exp_f32_e32 v175, v175
	v_pk_fma_f32 v[20:21], v[76:77], s[36:37], v[8:9] op_sel_hi:[1,0,1]
	v_pk_add_f32 v[174:175], v[174:175], 1.0 op_sel_hi:[1,0]
	s_nop 0
	v_rcp_f32_e32 v174, v174
	v_rcp_f32_e32 v175, v175
	v_min_f32_e32 v21, 0x40e00000, v21
	v_min_f32_e32 v20, 0x40e00000, v20
	v_pk_mul_f32 v[18:19], v[18:19], v[174:175]
	v_pk_mul_f32 v[174:175], v[20:21], s[78:79] op_sel_hi:[1,0]
	v_pk_mul_f32 v[18:19], v[172:173], v[18:19]
	v_exp_f32_e32 v174, v174
	v_exp_f32_e32 v175, v175
	v_cvt_pk_fp8_f32 v149, v18, v19 op_sel:[0,0,1]
	v_add_co_u32_e32 v18, vcc, s20, v16
	v_pk_add_f32 v[174:175], v[174:175], 1.0 op_sel_hi:[1,0]
	s_nop 0
	v_addc_co_u32_e32 v19, vcc, 0, v17, vcc
	v_rcp_f32_e32 v174, v174
	v_rcp_f32_e32 v175, v175
	v_pk_fma_f32 v[172:173], v[44:45], s[36:37], v[12:13] op_sel_hi:[1,0,1]
	v_lshl_add_u64 v[146:147], v[18:19], 0, v[152:153]
	v_pk_fma_f32 v[18:19], v[78:79], s[36:37], v[10:11] op_sel_hi:[1,0,1]
	v_med3_f32 v173, v173, s47, v190
	v_med3_f32 v172, v172, s47, v190
	v_pk_mul_f32 v[20:21], v[20:21], v[174:175]
	v_pk_fma_f32 v[172:173], v[172:173], 4.0, 4.0 op_sel_hi:[1,0,0]
	v_min_f32_e32 v19, 0x40e00000, v19
	v_min_f32_e32 v18, 0x40e00000, v18
	v_pk_mul_f32 v[20:21], v[172:173], v[20:21]
	v_pk_mul_f32 v[172:173], v[18:19], s[78:79] op_sel_hi:[1,0]
	v_pk_fma_f32 v[22:23], v[46:47], s[36:37], v[14:15] op_sel_hi:[1,0,1]
	v_exp_f32_e32 v172, v172
	v_exp_f32_e32 v173, v173
	v_med3_f32 v23, v23, s47, v190
	v_med3_f32 v22, v22, s47, v190
; #define LAS __attribute__((address_space(3)))
; template <bool EMU> __device__ __forceinline__ float e2m3q(float y) { if constexpr (EMU) { y = fminf(fmaxf(y, -7.5f), 7.5f); return fabsf(y) < 1.f ? rintf(y * 8.f) * 0.125f : y; } else return y; }
;     static __device__ __forceinline__ f32x2 act2(f32x2 g, f32x2 l) {
;         g = __builtin_elementwise_min(g, (f32x2){7.f, 7.f}); l = __builtin_elementwise_min(__builtin_elementwise_max(l, (f32x2){-7.f, -7.f}), (f32x2){7.f, 7.f});
;         const f32x2 t = g * (-1.702f * 1.44269504089f); f32x2 e; e.x = __builtin_amdgcn_exp2f(t.x); e.y = __builtin_amdgcn_exp2f(t.y);
;         const f32x2 d = e + 1.0f; f32x2 r; r.x = __builtin_amdgcn_rcpf(d.x); r.y = __builtin_amdgcn_rcpf(d.y);
;         return (g * r) * (l * QS_ACT + QS_ACT);
;     }
;     __device__ __forceinline__ void operator()(const f32x4 (&acc)[2][2][4][2], const UnitD& u, int wr, int wc, int fr, int fq) const {
;         const int row0 = u.r0 + wr * 64 + fr, col0 = u.c0 + wc * 32 + 8 * fq;
;         const LAS float* bg = bl_lds + u.ui * 256 + wc * 32 + 8 * fq; const LAS float* bl = bg + 128;
;         f32x4 bgv[2], blv[2];
; #pragma unroll
;         for (int n = 0; n < 2; ++n) { bgv[n] = *(const LAS f32x4*)(bg + 4 * n); blv[n] = *(const LAS f32x4*)(bl + 4 * n); }
;         constexpr float SC = 1.f / (QS_X1 * QS_WUP);
; #pragma unroll
;         for (int ai = 0; ai < 2; ++ai)
; #pragma unroll
;             for (int m = 0; m < 4; ++m) { unsigned char* rowp = H + (size_t)(row0 + ai * 128 + m * 16) * DM + col0; u32x2 w;
; #pragma unroll
;                 for (int n = 0; n < 2; ++n) { const f32x4 g = acc[ai][0][m][n] * SC + bgv[n], l = acc[ai][1][m][n] * SC + blv[n];
;                     const f32x2 o0 = act2((f32x2){g[0], g[1]}, (f32x2){l[0], l[1]}), o1 = act2((f32x2){g[2], g[3]}, (f32x2){l[2], l[3]});
;                     int r = 0; r = __builtin_amdgcn_cvt_pk_fp8_f32(e2m3q<EMU_DOWN != 0>(o0.x), e2m3q<EMU_DOWN != 0>(o0.y), r, false); r = __builtin_amdgcn_cvt_pk_fp8_f32(e2m3q<EMU_DOWN != 0>(o1.x), e2m3q<EMU_DOWN != 0>(o1.y), r, true);
;                     if (n == 0) w.x = (unsigned)r; else w.y = (unsigned)r; }
;                 *(u32x2*)rowp = w; }
	v_pk_fma_f32 v[22:23], v[22:23], 4.0, 4.0 op_sel_hi:[1,0,0]
	v_pk_add_f32 v[172:173], v[172:173], 1.0 op_sel_hi:[1,0]
	v_pk_fma_f32 v[174:175], v[40:41], s[36:37], v[4:5] op_sel_hi:[1,0,1]
	v_rcp_f32_e32 v172, v172
	v_rcp_f32_e32 v173, v173
	v_med3_f32 v175, v175, s47, v190
	v_med3_f32 v174, v174, s47, v190
	v_pk_fma_f32 v[174:175], v[174:175], 4.0, 4.0 op_sel_hi:[1,0,0]
	v_pk_mul_f32 v[18:19], v[18:19], v[172:173]
	v_pk_fma_f32 v[172:173], v[42:43], s[36:37], v[6:7] op_sel_hi:[1,0,1]
	v_pk_mul_f32 v[18:19], v[22:23], v[18:19]
	v_cvt_pk_fp8_f32 v150, v20, v21
	v_pk_fma_f32 v[20:21], v[72:73], s[36:37], v[0:1] op_sel_hi:[1,0,1]
	v_min_f32_e32 v21, 0x40e00000, v21
	v_min_f32_e32 v20, 0x40e00000, v20
	v_pk_mul_f32 v[176:177], v[20:21], s[78:79] op_sel_hi:[1,0]
	v_cvt_pk_fp8_f32 v150, v18, v19 op_sel:[0,0,1]
	v_exp_f32_e32 v176, v176
	v_exp_f32_e32 v177, v177
	v_pk_fma_f32 v[18:19], v[74:75], s[36:37], v[2:3] op_sel_hi:[1,0,1]
	v_med3_f32 v173, v173, s47, v190
	v_min_f32_e32 v19, 0x40e00000, v19
	v_pk_add_f32 v[176:177], v[176:177], 1.0 op_sel_hi:[1,0]
	v_min_f32_e32 v18, 0x40e00000, v18
	v_rcp_f32_e32 v176, v176
	v_rcp_f32_e32 v177, v177
	v_med3_f32 v172, v172, s47, v190
	v_pk_fma_f32 v[172:173], v[172:173], 4.0, 4.0 op_sel_hi:[1,0,0]
	s_mov_b32 s20, 0x24000
	v_pk_mul_f32 v[20:21], v[20:21], v[176:177]
	v_pk_mul_f32 v[20:21], v[174:175], v[20:21]
	v_pk_mul_f32 v[174:175], v[18:19], s[78:79] op_sel_hi:[1,0]
	v_cvt_pk_fp8_f32 v151, v20, v21
	v_exp_f32_e32 v174, v174
	v_exp_f32_e32 v175, v175
	v_pk_fma_f32 v[20:21], v[68:69], s[36:37], v[8:9] op_sel_hi:[1,0,1]
	v_pk_fma_f32 v[8:9], v[60:61], s[36:37], v[8:9] op_sel_hi:[1,0,1]
	v_min_f32_e32 v21, 0x40e00000, v21
	v_pk_add_f32 v[174:175], v[174:175], 1.0 op_sel_hi:[1,0]
	v_min_f32_e32 v20, 0x40e00000, v20
	v_rcp_f32_e32 v174, v174
	v_rcp_f32_e32 v175, v175
	v_min_f32_e32 v9, 0x40e00000, v9
	v_min_f32_e32 v8, 0x40e00000, v8
	v_pk_mul_f32 v[18:19], v[18:19], v[174:175]
	v_pk_mul_f32 v[174:175], v[20:21], s[78:79] op_sel_hi:[1,0]
	v_pk_mul_f32 v[18:19], v[172:173], v[18:19]
	v_exp_f32_e32 v174, v174
	v_exp_f32_e32 v175, v175
	v_cvt_pk_fp8_f32 v151, v18, v19 op_sel:[0,0,1]
	v_add_co_u32_e32 v18, vcc, s20, v16
	v_pk_add_f32 v[174:175], v[174:175], 1.0 op_sel_hi:[1,0]
	s_nop 0
	v_addc_co_u32_e32 v19, vcc, 0, v17, vcc
	v_rcp_f32_e32 v174, v174
	v_rcp_f32_e32 v175, v175
	v_pk_fma_f32 v[172:173], v[36:37], s[36:37], v[12:13] op_sel_hi:[1,0,1]
	v_permlane16_swap_b32_e32 v148, v150
	v_permlane16_swap_b32_e32 v149, v151
	global_store_dwordx4 v[146:147], v[148:151], off
	v_pk_fma_f32 v[18:19], v[70:71], s[36:37], v[10:11] op_sel_hi:[1,0,1]
	v_med3_f32 v173, v173, s47, v190
	v_med3_f32 v172, v172, s47, v190
	v_pk_mul_f32 v[20:21], v[20:21], v[174:175]
	v_pk_fma_f32 v[172:173], v[172:173], 4.0, 4.0 op_sel_hi:[1,0,0]
	v_min_f32_e32 v19, 0x40e00000, v19
	v_min_f32_e32 v18, 0x40e00000, v18
	v_pk_mul_f32 v[20:21], v[172:173], v[20:21]
	v_pk_mul_f32 v[172:173], v[18:19], s[78:79] op_sel_hi:[1,0]
	v_pk_fma_f32 v[22:23], v[38:39], s[36:37], v[14:15] op_sel_hi:[1,0,1]
	v_exp_f32_e32 v172, v172
	v_exp_f32_e32 v173, v173
	v_med3_f32 v23, v23, s47, v190
	v_med3_f32 v22, v22, s47, v190
	v_pk_fma_f32 v[22:23], v[22:23], 4.0, 4.0 op_sel_hi:[1,0,0]
	v_pk_add_f32 v[172:173], v[172:173], 1.0 op_sel_hi:[1,0]
	v_pk_fma_f32 v[174:175], v[32:33], s[36:37], v[4:5] op_sel_hi:[1,0,1]
	v_rcp_f32_e32 v172, v172
	v_rcp_f32_e32 v173, v173
	v_med3_f32 v175, v175, s47, v190
	v_med3_f32 v174, v174, s47, v190
	v_pk_fma_f32 v[174:175], v[174:175], 4.0, 4.0 op_sel_hi:[1,0,0]
	v_pk_mul_f32 v[18:19], v[18:19], v[172:173]
	v_pk_fma_f32 v[172:173], v[34:35], s[36:37], v[6:7] op_sel_hi:[1,0,1]
	v_pk_mul_f32 v[18:19], v[22:23], v[18:19]
	v_cvt_pk_fp8_f32 v148, v20, v21
	v_pk_fma_f32 v[20:21], v[64:65], s[36:37], v[0:1] op_sel_hi:[1,0,1]
	v_min_f32_e32 v21, 0x40e00000, v21
	v_min_f32_e32 v20, 0x40e00000, v20
	v_pk_mul_f32 v[176:177], v[20:21], s[78:79] op_sel_hi:[1,0]
	v_cvt_pk_fp8_f32 v148, v18, v19 op_sel:[0,0,1]
; #define LAS __attribute__((address_space(3)))
; template <bool EMU> __device__ __forceinline__ float e2m3q(float y) { if constexpr (EMU) { y = fminf(fmaxf(y, -7.5f), 7.5f); return fabsf(y) < 1.f ? rintf(y * 8.f) * 0.125f : y; } else return y; }
;     static __device__ __forceinline__ f32x2 act2(f32x2 g, f32x2 l) {
;         g = __builtin_elementwise_min(g, (f32x2){7.f, 7.f}); l = __builtin_elementwise_min(__builtin_elementwise_max(l, (f32x2){-7.f, -7.f}), (f32x2){7.f, 7.f});
;         const f32x2 t = g * (-1.702f * 1.44269504089f); f32x2 e; e.x = __builtin_amdgcn_exp2f(t.x); e.y = __builtin_amdgcn_exp2f(t.y);
;         const f32x2 d = e + 1.0f; f32x2 r; r.x = __builtin_amdgcn_rcpf(d.x); r.y = __builtin_amdgcn_rcpf(d.y);
;         return (g * r) * (l * QS_ACT + QS_ACT);
;     }
;     __device__ __forceinline__ void operator()(const f32x4 (&acc)[2][2][4][2], const UnitD& u, int wr, int wc, int fr, int fq) const {
;         const int row0 = u.r0 + wr * 64 + fr, col0 = u.c0 + wc * 32 + 8 * fq;
;         const LAS float* bg = bl_lds + u.ui * 256 + wc * 32 + 8 * fq; const LAS float* bl = bg + 128;
;         f32x4 bgv[2], blv[2];
; #pragma unroll
;         for (int n = 0; n < 2; ++n) { bgv[n] = *(const LAS f32x4*)(bg + 4 * n); blv[n] = *(const LAS f32x4*)(bl + 4 * n); }
;         constexpr float SC = 1.f / (QS_X1 * QS_WUP);
; #pragma unroll
;         for (int ai = 0; ai < 2; ++ai)
; #pragma unroll
;             for (int m = 0; m < 4; ++m) { unsigned char* rowp = H + (size_t)(row0 + ai * 128 + m * 16) * DM + col0; u32x2 w;
; #pragma unroll
;                 for (int n = 0; n < 2; ++n) { const f32x4 g = acc[ai][0][m][n] * SC + bgv[n], l = acc[ai][1][m][n] * SC + blv[n];
;                     const f32x2 o0 = act2((f32x2){g[0], g[1]}, (f32x2){l[0], l[1]}), o1 = act2((f32x2){g[2], g[3]}, (f32x2){l[2], l[3]});
;                     int r = 0; r = __builtin_amdgcn_cvt_pk_fp8_f32(e2m3q<EMU_DOWN != 0>(o0.x), e2m3q<EMU_DOWN != 0>(o0.y), r, false); r = __builtin_amdgcn_cvt_pk_fp8_f32(e2m3q<EMU_DOWN != 0>(o1.x), e2m3q<EMU_DOWN != 0>(o1.y), r, true);
;                     if (n == 0) w.x = (unsigned)r; else w.y = (unsigned)r; }
;                 *(u32x2*)rowp = w; }
	v_exp_f32_e32 v176, v176
	v_exp_f32_e32 v177, v177
	v_pk_fma_f32 v[18:19], v[66:67], s[36:37], v[2:3] op_sel_hi:[1,0,1]
	v_med3_f32 v173, v173, s47, v190
	v_min_f32_e32 v19, 0x40e00000, v19
	v_pk_add_f32 v[176:177], v[176:177], 1.0 op_sel_hi:[1,0]
	v_min_f32_e32 v18, 0x40e00000, v18
	v_rcp_f32_e32 v176, v176
	v_rcp_f32_e32 v177, v177
	v_med3_f32 v172, v172, s47, v190
	v_pk_fma_f32 v[172:173], v[172:173], 4.0, 4.0 op_sel_hi:[1,0,0]
	s_mov_b32 s20, 0x28000
	v_pk_mul_f32 v[20:21], v[20:21], v[176:177]
	v_pk_fma_f32 v[12:13], v[28:29], s[36:37], v[12:13] op_sel_hi:[1,0,1]
	v_pk_mul_f32 v[20:21], v[174:175], v[20:21]
	v_pk_mul_f32 v[174:175], v[18:19], s[78:79] op_sel_hi:[1,0]
	v_cvt_pk_fp8_f32 v149, v20, v21
	v_exp_f32_e32 v174, v174
	v_exp_f32_e32 v175, v175
	v_pk_fma_f32 v[10:11], v[62:63], s[36:37], v[10:11] op_sel_hi:[1,0,1]
	v_med3_f32 v13, v13, s47, v190
	v_med3_f32 v12, v12, s47, v190
	v_pk_add_f32 v[174:175], v[174:175], 1.0 op_sel_hi:[1,0]
	v_pk_fma_f32 v[14:15], v[30:31], s[36:37], v[14:15] op_sel_hi:[1,0,1]
	v_rcp_f32_e32 v174, v174
	v_rcp_f32_e32 v175, v175
	v_pk_fma_f32 v[12:13], v[12:13], 4.0, 4.0 op_sel_hi:[1,0,0]
	v_min_f32_e32 v11, 0x40e00000, v11
	v_min_f32_e32 v10, 0x40e00000, v10
	v_pk_mul_f32 v[18:19], v[18:19], v[174:175]
	v_pk_fma_f32 v[0:1], v[56:57], s[36:37], v[0:1] op_sel_hi:[1,0,1]
	v_pk_mul_f32 v[18:19], v[172:173], v[18:19]
	v_min_f32_e32 v1, 0x40e00000, v1
	v_cvt_pk_fp8_f32 v149, v18, v19 op_sel:[0,0,1]
	v_add_co_u32_e32 v18, vcc, s20, v16
	v_min_f32_e32 v0, 0x40e00000, v0
	s_nop 0
	v_addc_co_u32_e32 v19, vcc, 0, v17, vcc
	v_lshl_add_u64 v[146:147], v[18:19], 0, v[152:153]
	v_pk_mul_f32 v[18:19], v[8:9], s[78:79] op_sel_hi:[1,0]
	v_pk_fma_f32 v[4:5], v[24:25], s[36:37], v[4:5] op_sel_hi:[1,0,1]
	v_exp_f32_e32 v18, v18
	v_exp_f32_e32 v19, v19
	v_pk_fma_f32 v[2:3], v[58:59], s[36:37], v[2:3] op_sel_hi:[1,0,1]
	v_med3_f32 v5, v5, s47, v190
	v_med3_f32 v4, v4, s47, v190
	v_pk_add_f32 v[18:19], v[18:19], 1.0 op_sel_hi:[1,0]
	v_pk_fma_f32 v[6:7], v[26:27], s[36:37], v[6:7] op_sel_hi:[1,0,1]
	v_rcp_f32_e32 v18, v18
	v_rcp_f32_e32 v19, v19
	v_pk_fma_f32 v[4:5], v[4:5], 4.0, 4.0 op_sel_hi:[1,0,0]
	v_min_f32_e32 v3, 0x40e00000, v3
	v_min_f32_e32 v2, 0x40e00000, v2
	v_pk_mul_f32 v[8:9], v[8:9], v[18:19]
	v_pk_mul_f32 v[8:9], v[12:13], v[8:9]
	v_med3_f32 v13, v15, s47, v190
	v_med3_f32 v12, v14, s47, v190
	v_pk_mul_f32 v[14:15], v[10:11], s[78:79] op_sel_hi:[1,0]
	v_pk_fma_f32 v[12:13], v[12:13], 4.0, 4.0 op_sel_hi:[1,0,0]
	v_exp_f32_e32 v14, v14
	v_exp_f32_e32 v15, v15
	s_nop 0
	v_pk_add_f32 v[14:15], v[14:15], 1.0 op_sel_hi:[1,0]
	s_nop 0
	v_rcp_f32_e32 v14, v14
	v_rcp_f32_e32 v15, v15
	s_nop 0
	v_pk_mul_f32 v[10:11], v[10:11], v[14:15]
	v_pk_mul_f32 v[10:11], v[12:13], v[10:11]
	v_cvt_pk_fp8_f32 v150, v8, v9
	v_pk_mul_f32 v[8:9], v[0:1], s[78:79] op_sel_hi:[1,0]
	v_exp_f32_e32 v8, v8
	v_exp_f32_e32 v9, v9
	v_cvt_pk_fp8_f32 v150, v10, v11 op_sel:[0,0,1]
	v_pk_add_f32 v[8:9], v[8:9], 1.0 op_sel_hi:[1,0]
	s_nop 0
	v_rcp_f32_e32 v8, v8
	v_rcp_f32_e32 v9, v9
	s_nop 0
	v_pk_mul_f32 v[0:1], v[0:1], v[8:9]
	v_pk_mul_f32 v[0:1], v[4:5], v[0:1]
	v_med3_f32 v5, v7, s47, v190
	v_med3_f32 v4, v6, s47, v190
	v_pk_mul_f32 v[6:7], v[2:3], s[78:79] op_sel_hi:[1,0]
	v_cvt_pk_fp8_f32 v151, v0, v1
	v_exp_f32_e32 v6, v6
	v_exp_f32_e32 v7, v7
	v_pk_fma_f32 v[4:5], v[4:5], 4.0, 4.0 op_sel_hi:[1,0,0]
	v_add_co_u32_e32 v0, vcc, 0x2c000, v16
	v_pk_add_f32 v[6:7], v[6:7], 1.0 op_sel_hi:[1,0]
	s_nop 0
	v_addc_co_u32_e32 v1, vcc, 0, v17, vcc
	v_rcp_f32_e32 v6, v6
	v_rcp_f32_e32 v7, v7
	s_andn2_b64 vcc, exec, s[16:17]
	v_pk_mul_f32 v[2:3], v[2:3], v[6:7]
	v_pk_mul_f32 v[2:3], v[4:5], v[2:3]
	s_nop 0
	v_cvt_pk_fp8_f32 v151, v2, v3 op_sel:[0,0,1]
	s_nop 1
	v_permlane16_swap_b32_e32 v148, v150
	v_permlane16_swap_b32_e32 v149, v151
	global_store_dwordx4 v[146:147], v[148:151], off
	s_cbranch_vccnz .LBB0_759
	s_andn2_b64 vcc, exec, s[4:5]
	s_mov_b32 s86, 0x2f9636c4
	s_cbranch_vccnz .LBB0_758
	s_barrier
